# plus expert-weight conversion split retuned: 200 more blocks on the in_proj spare workgroups, 200 fewer inside each mixer phase
# speedup vs baseline: 1.0091x; 1.0025x over previous
.LBB0_310:
	s_lshl_b32 s4, s2, 3
	v_writelane_b32 v254, s4, 7
	s_lshl_b32 s4, s3, 3
	v_writelane_b32 v254, s4, 8
	s_lshl_b32 s4, s2, 9
	s_lshl_b32 s62, s3, 9
	s_cmp_eq_u32 s2, 0
	v_writelane_b32 v254, s4, 9
	s_cselect_b64 s[4:5], -1, 0
	v_writelane_b32 v254, s4, 10
	s_lshl_b32 s8, s2, 5
	s_and_b32 s14, s87, 31
	v_writelane_b32 v254, s5, 11
	s_mul_i32 s4, s2, 0x6b
	s_add_i32 s7, s4, 0xffffd954
	s_ashr_i32 s11, s87, 5
	s_lshl_b32 s4, s2, 4
	s_lshl_b32 s66, s3, 4
	s_cmpk_lt_i32 s2, 0x100
	v_writelane_b32 v254, s4, 12
	s_cselect_b64 s[4:5], -1, 0
	v_writelane_b32 v254, s4, 13
	s_movk_i32 s64, 0x80
	s_movk_i32 s65, 0xff00
	v_writelane_b32 v254, s5, 14
	s_not_b32 s4, s2
	s_add_i32 s4, s3, s4
	s_cmpk_lt_i32 s4, 0x80
	v_writelane_b32 v254, s4, 15
	s_cselect_b64 s[4:5], -1, 0
	s_and_b32 s9, s87, 3
	v_writelane_b32 v254, s4, 16
	s_cmpk_lt_i32 s2, 0x200
	s_movk_i32 s56, 0x1000
	v_writelane_b32 v254, s5, 17
	s_cselect_b64 s[4:5], -1, 0
	v_writelane_b32 v254, s4, 18
	s_lshl_b32 s74, s3, 5
	s_movk_i32 s77, 0x4400
	v_writelane_b32 v254, s5, 19
	s_lshl_b32 s4, s2, 2
	s_and_b32 s4, s4, 0xffffff00
	v_writelane_b32 v254, s4, 20
	s_lshl_b32 s4, s2, 6
	s_and_b32 s6, s4, 0xfc0
	s_cmp_gt_i32 s3, 0
	v_writelane_b32 v254, s4, 21
	s_cselect_b64 s[4:5], -1, 0
	v_writelane_b32 v254, s4, 22
	s_ashr_i32 s12, s87, 2
	s_mov_b32 s10, s12
	v_writelane_b32 v254, s5, 23
	s_ashr_i32 s4, s87, 3
	v_writelane_b32 v254, s4, 24
	s_and_b32 s5, s87, 7
	s_lshl_b32 s4, s5, 7
	v_writelane_b32 v254, s5, 25
	s_lshl_b32 s5, s5, 18
	v_writelane_b32 v254, s5, 26
	s_ashr_i32 s13, s12, 31
	v_writelane_b32 v254, s10, 27
	s_lshl_b64 s[12:13], s[12:13], 18
	s_lshl_b32 s5, s9, 8
	v_writelane_b32 v254, s11, 28
	v_writelane_b32 v254, s12, 29
	s_mov_b32 s38, 0x78787879
	s_movk_i32 s39, 0xef00
	v_writelane_b32 v254, s13, 30
	v_writelane_b32 v254, s9, 31
	s_lshl_b32 s9, s9, 18
	s_cmpk_lt_i32 s2, 0x84
	v_writelane_b32 v254, s9, 32
	s_cselect_b32 s9, 32, 0x6b
	v_writelane_b32 v254, s9, 33
	v_writelane_b32 v254, s8, 34
	s_cselect_b32 s7, s8, s7
	v_writelane_b32 v254, s7, 35
	s_add_i32 s7, s3, -1
	s_cmp_gt_u32 s7, 6
	s_cselect_b64 s[8:9], -1, 0
	s_abs_i32 s12, s3
	v_cvt_f32_u32_e32 v1, s12
	v_writelane_b32 v254, s8, 36
	s_sub_i32 s7, 0, s12
	s_and_b32 s76, s3, 0x7ffffff8
	v_rcp_iflag_f32_e32 v1, v1
	v_writelane_b32 v254, s9, 37
	s_ashr_i32 s13, s3, 31
	s_mov_b32 s59, 0x800000
	v_mul_f32_e32 v1, 0x4f7ffffe, v1
	v_cvt_u32_f32_e32 v1, v1
	v_mov_b32_e32 v205, 1
	v_mov_b32_e32 v221, 0x1400
	v_mov_b32_e32 v204, 0x20200
	v_readfirstlane_b32 s8, v1
	s_mul_i32 s7, s7, s8
	s_mul_hi_u32 s7, s8, s7
	s_add_i32 s7, s8, s7
	v_writelane_b32 v254, s7, 38
	s_mul_hi_u32 s7, s7, 0x6d3
	s_mul_i32 s8, s7, s12
	s_sub_i32 s8, 0x6d3, s8
	s_add_i32 s9, s7, 1
	s_sub_i32 s10, s8, s12
	s_cmp_ge_u32 s8, s12
	s_cselect_b32 s7, s9, s7
	s_cselect_b32 s8, s10, s8
	s_add_i32 s9, s7, 1
	s_cmp_ge_u32 s8, s12
	s_cselect_b32 s7, s9, s7
	s_xor_b32 s7, s7, s13
	s_sub_i32 s7, s7, s13
	s_mul_i32 s8, s7, s3
	s_sub_i32 s8, 0x6d3, s8
	s_mul_i32 s9, s7, s87
	s_min_i32 s10, s87, s8
	v_writelane_b32 v254, s12, 39
	s_add_i32 s9, s9, s10
	v_writelane_b32 v254, s13, 40
	s_cmp_lt_i32 s87, s8
	v_writelane_b32 v254, s9, 41
	s_cselect_b64 s[8:9], -1, 0
	s_cmp_lg_u64 s[8:9], 0
	s_addc_u32 s7, s7, 0
	v_writelane_b32 v254, s7, 42
	s_lshl_b32 s7, s3, 1
	v_writelane_b32 v254, s7, 43
	s_add_i32 s7, s11, 17
	v_writelane_b32 v254, s7, 44
	s_lshl_b32 s7, s7, 4
	v_writelane_b32 v254, s7, 45
	s_lshl_b32 s7, s14, 4
	v_writelane_b32 v254, s14, 46
	s_add_i32 s8, s7, 0xd250
	v_writelane_b32 v254, s8, 47
	s_add_i32 s8, s11, 9
	v_writelane_b32 v254, s8, 48
	s_lshl_b32 s8, s8, 4
	v_writelane_b32 v254, s8, 49
	v_writelane_b32 v254, s11, 50
	s_add_i32 s8, s11, 1
	v_writelane_b32 v254, s8, 51
	s_or_b32 s8, s7, 0xfffffe00
	v_writelane_b32 v254, s8, 52
	s_lshl_b32 s8, s3, 6
	v_writelane_b32 v254, s8, 53
	s_add_i32 s7, s7, 0xa050
	v_writelane_b32 v254, s7, 54
	s_add_i32 s7, 0, 0x12000
	v_writelane_b32 v254, s7, 55
	s_add_i32 s7, 0, 0x27020
	v_writelane_b32 v254, s7, 56
	s_add_i32 s7, 0, 0x27024
	v_writelane_b32 v254, s7, 57
	s_add_i32 s7, 0, 0x25000
	v_writelane_b32 v254, s7, 58
	s_lshl_b32 s6, s6, 1
	v_writelane_b32 v254, s6, 59
	s_lshl_b32 s5, s5, 2
	v_writelane_b32 v254, s5, 60
	s_add_i32 s5, 0, 0x25400
	v_writelane_b32 v254, s5, 61
	s_add_i32 s5, 0, 0x10200
	v_writelane_b32 v254, s5, 62
	s_add_i32 s5, 0, 0x20100
	v_writelane_b32 v254, s5, 63
	s_add_i32 s5, 0, 0x20010
	v_writelane_b32 v255, s5, 0
	s_add_i32 s5, 0, 0x20110
	v_writelane_b32 v255, s5, 1
	s_add_i32 s5, 0, 0x20020
	v_writelane_b32 v255, s5, 2
	s_add_i32 s5, 0, 0x20120
	v_writelane_b32 v255, s5, 3
	s_add_i32 s5, 0, 0x20030
	v_writelane_b32 v255, s5, 4
	s_add_i32 s5, 0, 0x20130
	v_writelane_b32 v255, s5, 5
	s_add_i32 s5, 0, 0x20040
	v_writelane_b32 v255, s5, 6
	s_add_i32 s5, 0, 0x20140
	v_writelane_b32 v255, s5, 7
	s_add_i32 s5, 0, 0x20050
	v_writelane_b32 v255, s5, 8
	s_add_i32 s5, 0, 0x20150
	v_writelane_b32 v255, s5, 9
	s_add_i32 s5, 0, 0x20060
	v_writelane_b32 v255, s5, 10
	s_add_i32 s5, 0, 0x20160
	v_writelane_b32 v255, s5, 11
	s_add_i32 s5, 0, 0x20070
	v_writelane_b32 v255, s5, 12
	s_add_i32 s5, 0, 0x20170
	v_writelane_b32 v255, s5, 13
	s_add_i32 s5, 0, 0x20180
	v_writelane_b32 v255, s5, 14
	s_add_i32 s5, 0, 0x20084
	v_writelane_b32 v255, s5, 15
	s_add_i32 s5, 0, 0x20024
	v_writelane_b32 v255, s5, 16
	s_add_i32 s5, 0, 0x2002c
	v_writelane_b32 v255, s5, 17
	s_add_i32 s5, 0, 0x20034
	v_writelane_b32 v255, s5, 18
	s_add_i32 s5, 0, 0x2003c
	v_writelane_b32 v255, s5, 19
	s_add_i32 s5, 0, 0x20044
	v_writelane_b32 v255, s5, 20
	s_add_i32 s5, 0, 0x2004c
	v_writelane_b32 v255, s5, 21
	s_add_i32 s5, 0, 0x20054
	v_writelane_b32 v255, s5, 22
	s_add_i32 s5, 0, 0x2005c
	v_writelane_b32 v255, s5, 23
	s_add_i32 s5, 0, 0x20064
	v_writelane_b32 v255, s5, 24
	s_add_i32 s5, 0, 0x2006c
	v_writelane_b32 v255, s5, 25
	s_add_i32 s5, 0, 0x20074
	v_writelane_b32 v255, s5, 26
	s_add_i32 s5, 0, 0x2007c
	v_writelane_b32 v255, s5, 27
	s_add_i32 s5, 0, 0x20800
	v_writelane_b32 v255, s5, 28
	s_lshl_b32 s4, s4, 2
	v_writelane_b32 v255, s4, 29
	s_ashr_i32 s63, s62, 31
	s_ashr_i32 s67, s66, 31
	v_writelane_b32 v255, s5, 30
	v_cmp_eq_u32_e64 s[4:5], 0, v0
	s_mov_b32 s6, s74
	s_add_i32 s84, 0, 0x20004
	v_writelane_b32 v255, s4, 31
	s_add_i32 s69, 0, 0x2000c
	s_add_i32 s68, 0, 0x20014
	v_writelane_b32 v255, s5, 32
	s_lshl_b64 s[4:5], s[62:63], 2
	v_writelane_b32 v255, s4, 33
	s_add_i32 s49, 0, 0x2001c
	v_mov_b32_e32 v1, 0
	v_writelane_b32 v255, s5, 34
	s_lshl_b64 s[4:5], s[66:67], 12
	v_writelane_b32 v255, s4, 35
	v_mov_b32_e32 v220, 0xff800000
	s_movk_i32 s47, 0x3ff
	v_writelane_b32 v255, s5, 36
	v_writelane_b32 v255, s6, 37
	s_mov_b32 s83, 0x34400000
	s_mov_b32 s80, 0x36500000
	v_writelane_b32 v255, s7, 38
	s_mov_b32 s6, s62
	v_writelane_b32 v255, s6, 39
	s_movk_i32 s81, 0x7fff
	s_mov_b32 s57, 0x41000000
	v_writelane_b32 v255, s7, 40
	s_mov_b32 s6, s66
	v_writelane_b32 v255, s6, 41
	s_movk_i32 s33, 0xfefe
	s_mov_b32 s85, 0x900000
	v_writelane_b32 v255, s7, 42
	v_writelane_b32 v255, s76, 43
	v_writelane_b32 v255, s84, 44
	s_mov_b32 s72, 0xc0e00000
	s_mov_b32 s73, 0
	s_mov_b32 s71, 0
	s_mov_b64 s[4:5], -1
	s_mov_b64 s[78:79], 0x80
	s_mov_b32 s82, 0x3e38aa3b
	s_mov_b32 s88, 0xc01d265f
	s_mov_b32 s50, s69
	s_mov_b32 s86, s68
	s_mov_b32 s60, s49
	v_writelane_b32 v255, s87, 45
	s_branch .LBB0_314

.LBB0_561:
	s_and_b64 vcc, exec, s[16:17]
	s_cbranch_vccz .LBB0_711
	v_readlane_b32 s6, v254, 50
	v_readlane_b32 s7, v254, 46
	s_mul_i32 s6, s35, s6
	s_sub_i32 s7, s7, s36
	s_add_i32 s23, s7, s6
	s_lshl_b32 s22, s35, 3
	s_mov_b64 s[6:7], -1
	s_and_b64 vcc, exec, s[90:91]
	s_cbranch_vccz .LBB0_637
	v_mbcnt_lo_u32_b32 v66, -1, 0
	v_mbcnt_hi_u32_b32 v66, -1, v66
	s_getreg_b32 s6, hwreg(HW_REG_HW_ID, 0, 6)
	s_lshl_b32 s6, s6, 2
	s_and_b32 s6, s6, 0xfc
	s_or_b32 s6, s6, 0x27100
	v_mov_b32_e32 v0, s6
	ds_read_b32 v0, v0
	s_cmpk_gt_i32 s23, 0x3e7
	s_waitcnt lgkmcnt(0)
	v_readfirstlane_b32 s9, v0
	s_cbranch_scc1 .LBB0_636
	s_add_i32 s20, s23, 0xd45
	s_mul_hi_i32 s6, s20, 0x2aaaaaab
	s_lshr_b32 s7, s6, 31
	s_ashr_i32 s15, s6, 9
	s_add_i32 s15, s15, s7
	s_mul_i32 s16, s15, 0xfffff400
	s_add_i32 s16, s16, s20
	s_cmpk_gt_i32 s16, 0x7ff
	s_mov_b64 s[12:13], -1
	s_cbranch_scc0 .LBB0_566
	s_add_i32 s6, s16, 0xfffff800
	s_mov_b32 s10, 31
	s_lshl_b32 s7, s15, 5
	s_lshr_b32 s6, s6, 5
	s_lshl_b32 s24, s20, 8
	s_ashr_i32 s11, s10, 31
	s_add_i32 s6, s6, s7
	s_lshl_b32 s14, s20, 5
	s_and_b32 s8, s24, 0x300
	s_lshl_b64 s[10:11], s[10:11], 3
	s_add_u32 s10, s0, s10
	s_addc_u32 s11, s1, s11
	s_load_dwordx2 s[10:11], s[10:11], 0x0
	s_ashr_i32 s7, s6, 31
	s_lshl_b64 s[12:13], s[6:7], 20
	s_lshl_b64 s[6:7], s[6:7], 22
	s_waitcnt lgkmcnt(0)
	s_add_u32 s6, s10, s6
	s_mov_b32 s10, 35
	s_addc_u32 s7, s11, s7
	s_ashr_i32 s11, s10, 31
	s_lshl_b64 s[10:11], s[10:11], 3
	s_add_u32 s10, s0, s10
	s_addc_u32 s11, s1, s11
	s_load_dwordx2 s[10:11], s[10:11], 0x0
	s_waitcnt lgkmcnt(0)
	s_add_u32 s10, s10, s12
	s_addc_u32 s11, s11, s13
	s_add_u32 s10, s10, 0x12800000
	s_addc_u32 s11, s11, 0
	s_mov_b64 s[12:13], 0

.LBB0_571:
	v_ashrrev_i32_e32 v139, 31, v138
	v_lshlrev_b64 v[138:139], 10, v[138:139]
	s_add_i32 s30, s30, s27
	v_readlane_b32 s6, v254, 46
	v_lshl_add_u64 v[138:139], s[16:17], 0, v[138:139]
	s_add_i32 s24, s24, s25
	s_add_i32 s26, s26, s27
	s_add_i32 s36, s36, s28
	s_add_i32 s29, s29, s27
	s_add_i32 s6, s6, s30
	v_lshl_add_u64 v[138:139], v[138:139], 0, s[14:15]
	s_cmpk_gt_i32 s6, 0x112c
	v_lshl_add_u64 v[138:139], v[138:139], 0, v[136:137]
	s_cselect_b64 s[6:7], -1, 0
	s_waitcnt lgkmcnt(0)
	global_store_dwordx4 v[138:139], v[130:133], off

.LBB0_573:
	v_readlane_b32 s6, v254, 46
	s_add_i32 s6, s6, s29
	s_add_i32 s9, s20, s22
	s_add_i32 s7, s6, 0xd25
	s_cmpk_lt_i32 s7, 0x112d
	s_cselect_b64 s[18:19], -1, 0
	s_cmpk_gt_i32 s7, 0x112c
	s_cbranch_scc1 .LBB0_580
	s_mul_hi_i32 s7, s7, 0x2aaaaaab
	s_lshr_b32 s12, s7, 31
	s_ashr_i32 s20, s7, 9
	s_add_i32 s20, s20, s12
	s_mul_i32 s7, s20, 0xfffff400
	s_add_i32 s37, s6, s7
	s_add_i32 s21, s37, 0xd25
	s_cmpk_gt_i32 s21, 0x7ff
	s_mov_b64 s[14:15], -1
	s_cbranch_scc0 .LBB0_576
	s_addk_i32 s37, 0x525
	s_mov_b32 s14, 31
	s_lshl_b32 s6, s20, 5
	s_lshr_b32 s7, s37, 5
	s_ashr_i32 s15, s14, 31
	s_add_i32 s6, s7, s6
	s_lshl_b32 s13, s9, 5
	s_and_b32 s12, s24, 0x300
	s_lshl_b64 s[14:15], s[14:15], 3
	s_add_u32 s14, s0, s14
	s_addc_u32 s15, s1, s15
	s_load_dwordx2 s[14:15], s[14:15], 0x0
	s_ashr_i32 s7, s6, 31
	s_lshl_b64 s[16:17], s[6:7], 20
	s_lshl_b64 s[6:7], s[6:7], 22
	s_waitcnt lgkmcnt(0)
	s_add_u32 s6, s14, s6
	s_mov_b32 s14, 35
	s_addc_u32 s7, s15, s7
	s_ashr_i32 s15, s14, 31
	s_lshl_b64 s[14:15], s[14:15], 3
	s_add_u32 s14, s0, s14
	s_addc_u32 s15, s1, s15
	s_load_dwordx2 s[14:15], s[14:15], 0x0
	s_waitcnt lgkmcnt(0)
	s_add_u32 s14, s14, s16
	s_addc_u32 s15, s15, s17
	s_add_u32 s16, s14, 0x12800000
	s_addc_u32 s17, s15, 0
	s_mov_b64 s[14:15], 0

.LBB0_604:
	v_ashrrev_i32_e32 v139, 31, v138
	v_lshlrev_b64 v[138:139], 10, v[138:139]
	v_lshl_add_u64 v[138:139], s[10:11], 0, v[138:139]
	v_lshl_add_u64 v[138:139], v[138:139], 0, s[70:71]
	v_lshl_add_u64 v[138:139], v[138:139], 0, v[136:137]
	s_andn2_b64 vcc, exec, s[18:19]
	s_mov_b64 s[6:7], -1
	s_waitcnt lgkmcnt(0)
	global_store_dwordx4 v[138:139], v[130:133], off
	s_cbranch_vccnz .LBB0_572
	v_readlane_b32 s6, v254, 46
	s_add_i32 s6, s6, s26
	s_add_i32 s20, s9, s22
	s_add_i32 s7, s6, 0xd25
	s_cmpk_gt_i32 s7, 0x112c
	s_cbranch_scc1 .LBB0_612
	s_mul_hi_i32 s7, s7, 0x2aaaaaab
	s_lshr_b32 s8, s7, 31
	s_ashr_i32 s13, s7, 9
	s_add_i32 s13, s13, s8
	s_mul_i32 s7, s13, 0xfffff400
	s_add_i32 s21, s6, s7
	s_add_i32 s15, s21, 0xd25
	s_cmpk_gt_i32 s15, 0x7ff
	s_mov_b64 s[18:19], -1
	s_cbranch_scc0 .LBB0_608
	s_addk_i32 s21, 0x525
	s_mov_b32 s10, 31
	s_lshl_b32 s6, s13, 5
	s_lshr_b32 s7, s21, 5
	s_ashr_i32 s11, s10, 31
	s_add_i32 s6, s7, s6
	s_lshl_b32 s9, s20, 5
	s_and_b32 s8, s24, 0x300
	s_lshl_b64 s[10:11], s[10:11], 3
	s_add_u32 s10, s0, s10
	s_addc_u32 s11, s1, s11
	s_load_dwordx2 s[10:11], s[10:11], 0x0
	s_ashr_i32 s7, s6, 31
	s_lshl_b64 s[18:19], s[6:7], 20
	s_lshl_b64 s[6:7], s[6:7], 22
	s_waitcnt lgkmcnt(0)
	s_add_u32 s6, s10, s6
	s_mov_b32 s10, 35
	s_addc_u32 s7, s11, s7
	s_ashr_i32 s11, s10, 31
	s_lshl_b64 s[10:11], s[10:11], 3
	s_add_u32 s10, s0, s10
	s_addc_u32 s11, s1, s11
	s_load_dwordx2 s[10:11], s[10:11], 0x0
	s_waitcnt lgkmcnt(0)
	s_add_u32 s10, s10, s18
	s_addc_u32 s11, s11, s19
	s_add_u32 s10, s10, 0x12800000
	s_addc_u32 s11, s11, 0
	s_mov_b64 s[18:19], 0

.LBB0_637:
	s_andn2_b64 vcc, exec, s[6:7]
	s_cbranch_vccnz .LBB0_711
	v_mbcnt_lo_u32_b32 v66, -1, 0
	v_mbcnt_hi_u32_b32 v66, -1, v66
	s_getreg_b32 s6, hwreg(HW_REG_HW_ID, 0, 6)
	s_lshl_b32 s6, s6, 2
	s_and_b32 s6, s6, 0xfc
	s_or_b32 s6, s6, 0x27100
	v_mov_b32_e32 v0, s6
	ds_read_b32 v0, v0
	s_cmpk_gt_i32 s23, 0x351
	s_waitcnt lgkmcnt(0)
	v_readfirstlane_b32 s9, v0
	s_cbranch_scc1 .LBB0_711
	s_mul_hi_i32 s6, s23, 0x2aaaaaab
	s_lshr_b32 s7, s6, 31
	s_ashr_i32 s15, s6, 9
	s_add_i32 s15, s15, s7
	s_mul_i32 s16, s15, 0xfffff400
	s_add_i32 s16, s16, s23
	s_cmpk_gt_i32 s16, 0x7ff
	s_mov_b64 s[12:13], -1
	s_cbranch_scc0 .LBB0_641
	s_add_i32 s6, s16, 0xfffff800
	s_mov_b32 s10, 31
	s_lshl_b32 s7, s15, 5
	s_lshr_b32 s6, s6, 5
	s_lshl_b32 s24, s23, 8
	s_ashr_i32 s11, s10, 31
	s_add_i32 s6, s6, s7
	s_lshl_b32 s14, s23, 5
	s_and_b32 s8, s24, 0x300
	s_lshl_b64 s[10:11], s[10:11], 3
	s_add_u32 s10, s0, s10
	s_addc_u32 s11, s1, s11
	s_load_dwordx2 s[10:11], s[10:11], 0x0
	s_ashr_i32 s7, s6, 31
	s_lshl_b64 s[12:13], s[6:7], 20
	s_lshl_b64 s[6:7], s[6:7], 22
	s_waitcnt lgkmcnt(0)
	s_add_u32 s6, s10, s6
	s_mov_b32 s10, 35
	s_addc_u32 s7, s11, s7
	s_ashr_i32 s11, s10, 31
	s_lshl_b64 s[10:11], s[10:11], 3
	s_add_u32 s10, s0, s10
	s_addc_u32 s11, s1, s11
	s_load_dwordx2 s[10:11], s[10:11], 0x0
	s_waitcnt lgkmcnt(0)
	s_add_u32 s10, s10, s12
	s_addc_u32 s11, s11, s13
	s_add_u32 s10, s10, 0x12800000
	s_addc_u32 s11, s11, 0
	s_mov_b64 s[12:13], 0

.LBB0_646:
	v_ashrrev_i32_e32 v139, 31, v138
	v_lshlrev_b64 v[138:139], 10, v[138:139]
	s_add_i32 s35, s35, s27
	v_readlane_b32 s6, v254, 46
	v_lshl_add_u64 v[138:139], s[16:17], 0, v[138:139]
	s_add_i32 s24, s24, s25
	s_add_i32 s26, s26, s27
	s_add_i32 s37, s37, s29
	s_add_i32 s30, s30, s27
	s_add_i32 s6, s6, s35
	v_lshl_add_u64 v[138:139], v[138:139], 0, s[14:15]
	s_cmpk_gt_i32 s6, 0x351
	v_lshl_add_u64 v[138:139], v[138:139], 0, v[136:137]
	s_cselect_b64 s[6:7], -1, 0
	s_waitcnt lgkmcnt(0)
	global_store_dwordx4 v[138:139], v[130:133], off

.LBB0_648:
	v_readlane_b32 s6, v254, 46
	s_add_i32 s6, s6, s30
	s_add_i32 s9, s23, s22
	s_sub_i32 s7, s6, 32
	s_cmpk_lt_i32 s7, 0x352
	s_cselect_b64 s[18:19], -1, 0
	s_cmpk_gt_i32 s7, 0x351
	s_cbranch_scc1 .LBB0_655
	s_mul_hi_i32 s7, s7, 0x2aaaaaab
	s_lshr_b32 s12, s7, 31
	s_ashr_i32 s20, s7, 9
	s_add_i32 s20, s20, s12
	s_mul_i32 s7, s20, 0xfffff400
	s_add_i32 s23, s6, s7
	s_sub_i32 s21, s23, 32
	s_cmpk_gt_i32 s21, 0x7ff
	s_mov_b64 s[14:15], -1
	s_cbranch_scc0 .LBB0_651
	s_addk_i32 s23, 0xf7e0
	s_mov_b32 s14, 31
	s_lshl_b32 s6, s20, 5
	s_lshr_b32 s7, s23, 5
	s_ashr_i32 s15, s14, 31
	s_add_i32 s6, s7, s6
	s_lshl_b32 s13, s9, 5
	s_and_b32 s12, s24, 0x300
	s_lshl_b64 s[14:15], s[14:15], 3
	s_add_u32 s14, s0, s14
	s_addc_u32 s15, s1, s15
	s_load_dwordx2 s[14:15], s[14:15], 0x0
	s_ashr_i32 s7, s6, 31
	s_lshl_b64 s[16:17], s[6:7], 20
	s_lshl_b64 s[6:7], s[6:7], 22
	s_waitcnt lgkmcnt(0)
	s_add_u32 s6, s14, s6
	s_mov_b32 s14, 35
	s_addc_u32 s7, s15, s7
	s_ashr_i32 s15, s14, 31
	s_lshl_b64 s[14:15], s[14:15], 3
	s_add_u32 s14, s0, s14
	s_addc_u32 s15, s1, s15
	s_load_dwordx2 s[14:15], s[14:15], 0x0
	s_waitcnt lgkmcnt(0)
	s_add_u32 s14, s14, s16
	s_addc_u32 s15, s15, s17
	s_add_u32 s16, s14, 0x12800000
	s_addc_u32 s17, s15, 0
	s_mov_b64 s[14:15], 0

.LBB0_679:
	v_ashrrev_i32_e32 v139, 31, v138
	v_lshlrev_b64 v[138:139], 10, v[138:139]
	v_lshl_add_u64 v[138:139], s[10:11], 0, v[138:139]
	v_lshl_add_u64 v[138:139], v[138:139], 0, s[70:71]
	v_lshl_add_u64 v[138:139], v[138:139], 0, v[136:137]
	s_andn2_b64 vcc, exec, s[18:19]
	s_mov_b64 s[6:7], -1
	s_waitcnt lgkmcnt(0)
	global_store_dwordx4 v[138:139], v[130:133], off
	s_cbranch_vccnz .LBB0_647
	v_readlane_b32 s6, v254, 46
	s_add_i32 s6, s6, s26
	s_add_i32 s23, s9, s22
	s_sub_i32 s7, s6, 32
	s_cmpk_gt_i32 s7, 0x351
	s_cbranch_scc1 .LBB0_687
	s_mul_hi_i32 s7, s7, 0x2aaaaaab
	s_lshr_b32 s8, s7, 31
	s_ashr_i32 s13, s7, 9
	s_add_i32 s13, s13, s8
	s_mul_i32 s7, s13, 0xfffff400
	s_add_i32 s20, s6, s7
	s_sub_i32 s15, s20, 32
	s_cmpk_gt_i32 s15, 0x7ff
	s_mov_b64 s[18:19], -1
	s_cbranch_scc0 .LBB0_683
	s_addk_i32 s20, 0xf7e0
	s_mov_b32 s10, 31
	s_lshl_b32 s6, s13, 5
	s_lshr_b32 s7, s20, 5
	s_ashr_i32 s11, s10, 31
	s_add_i32 s6, s7, s6
	s_lshl_b32 s9, s23, 5
	s_and_b32 s8, s24, 0x300
	s_lshl_b64 s[10:11], s[10:11], 3
	s_add_u32 s10, s0, s10
	s_addc_u32 s11, s1, s11
	s_load_dwordx2 s[10:11], s[10:11], 0x0
	s_ashr_i32 s7, s6, 31
	s_lshl_b64 s[18:19], s[6:7], 20
	s_lshl_b64 s[6:7], s[6:7], 22
	s_waitcnt lgkmcnt(0)
	s_add_u32 s6, s10, s6
	s_mov_b32 s10, 35
	s_addc_u32 s7, s11, s7
	s_ashr_i32 s11, s10, 31
	s_lshl_b64 s[10:11], s[10:11], 3
	s_add_u32 s10, s0, s10
	s_addc_u32 s11, s1, s11
	s_load_dwordx2 s[10:11], s[10:11], 0x0
	s_waitcnt lgkmcnt(0)
	s_add_u32 s10, s10, s18
	s_addc_u32 s11, s11, s19
	s_add_u32 s10, s10, 0x12800000
	s_addc_u32 s11, s11, 0
	s_mov_b64 s[18:19], 0

.LBB0_922:
	s_andn2_b64 vcc, exec, s[54:55]
	s_mov_b32 s43, 0
	s_cbranch_vccnz .LBB0_924
	s_and_b64 s[6:7], s[4:5], exec
	s_movk_i32 s6, 0x352
	s_cselect_b32 s6, s6, 0x112d
	v_readlane_b32 s7, v254, 41
	s_add_i32 s43, s6, s7
